# agg1 layout D: 8 lanes per node (16 fp8 channels per lane), 8 nodes per wave, rolled stage loop, ds_swizzle index broadcast
# speedup vs baseline: 1.0315x; 1.0315x over previous
_Z11agg1_kernelPKDF16_PKfS2_PKiS4_S2_S2_PDF16_PfS6_i:
	s_load_dwordx8 s[4:11], s[0:1], 0x0
	s_load_dwordx8 s[12:19], s[0:1], 0x20
	s_load_dwordx4 s[20:23], s[0:1], 0x40
	s_load_dword s24, s[0:1], 0x50
	v_lshlrev_b32_e32 v32, 2, v0
	v_readfirstlane_b32 s25, v0
	s_lshl_b32 s26, s2, 5
	v_and_b32_e32 v64, 7, v0
	v_bfe_u32 v65, v0, 3, 3
	s_lshr_b32 s25, s25, 6
	s_lshl_b32 s27, s25, 3
	s_add_i32 s26, s26, s27
	v_lshlrev_b32_e32 v1, 1, v64
	v_add_u32_e32 v66, s26, v65
	s_waitcnt lgkmcnt(0)
	global_load_dword v33, v32, s[14:15]
	global_load_dword v34, v32, s[16:17]
	s_add_i32 s28, s24, -1
	v_cmp_gt_i32_e64 s[36:37], s24, v66
	v_min_i32_e32 v66, s28, v66
	v_lshlrev_b32_e32 v4, 2, v66
	global_load_dword v10, v4, s[10:11]
	global_load_dword v11, v4, s[10:11] offset:4
	v_lshlrev_b32_e32 v35, 2, v64
	v_lshl_or_b32 v35, v66, 5, v35
	global_load_dword v9, v35, s[8:9]
	s_cmp_le_i32 s24, s26
	s_waitcnt vmcnt(3)
	ds_write2st64_b32 v32, v33, v34 offset0:32 offset1:36
	s_waitcnt lgkmcnt(0)
	s_barrier
	s_cbranch_scc1 .Lagg_exit
	v_lshlrev_b32_e32 v3, 8, v64
	v_lshl_add_u32 v3, v65, 1, v3
	s_lshl_b32 s27, s25, 11
	v_add_u32_e32 v3, s27, v3
	v_lshlrev_b32_e32 v62, 6, v64
	v_add_u32_e32 v62, 0x2000, v62
	v_cmp_eq_u32_e64 s[34:35], 0, v64
	v_and_b32_e32 v32, 63, v0
	v_lshlrev_b32_e32 v32, 5, v32
	v_add_u32_e32 v63, s27, v32
	v_mov_b32_e32 v36, 0
	v_mov_b32_e32 v37, 0
	v_mov_b32_e32 v38, 0
	v_mov_b32_e32 v39, 0
	ds_write_b128 v63, v[36:39]
	ds_write_b128 v63, v[36:39] offset:16
	s_waitcnt vmcnt(1)
	v_sub_u32_e32 v11, v11, v10
	v_add_u32_e32 v11, 1, v11
	s_nop 1
	v_readlane_b32 s29, v11, 0
	v_readlane_b32 s40, v11, 8
	s_max_i32 s29, s29, s40
	v_readlane_b32 s40, v11, 16
	s_max_i32 s29, s29, s40
	v_readlane_b32 s40, v11, 24
	s_max_i32 s29, s29, s40
	v_readlane_b32 s40, v11, 32
	s_max_i32 s29, s29, s40
	v_readlane_b32 s40, v11, 40
	s_max_i32 s29, s29, s40
	v_readlane_b32 s40, v11, 48
	s_max_i32 s29, s29, s40
	v_readlane_b32 s40, v11, 56
	s_max_i32 s29, s29, s40
	v_add_u32_e32 v67, v10, v64
	v_lshlrev_b32_e32 v67, 2, v67
	v_mov_b32_e32 v5, s24
	v_mov_b32_e32 v6, s24
	v_mov_b32_e32 v7, s24
	v_mov_b32_e32 v8, s24
	v_cndmask_b32_e64 v5, v5, v66, s[34:35]
	v_cmp_gt_i32_e32 vcc, v11, v64
	s_andn2_b64 s[40:41], vcc, s[34:35]
	s_and_saveexec_b64 s[32:33], s[40:41]
	global_load_dword v5, v67, s[12:13] offset:-4
	s_mov_b64 exec, s[32:33]
	v_add_u32_e32 v68, 8, v64
	v_cmp_gt_i32_e32 vcc, v11, v68
	s_and_saveexec_b64 s[32:33], vcc
	global_load_dword v6, v67, s[12:13] offset:28
	s_mov_b64 exec, s[32:33]
	v_add_u32_e32 v68, 16, v64
	v_cmp_gt_i32_e32 vcc, v11, v68
	s_and_saveexec_b64 s[32:33], vcc
	global_load_dword v7, v67, s[12:13] offset:60
	s_mov_b64 exec, s[32:33]
	v_add_u32_e32 v68, 24, v64
	v_cmp_gt_i32_e32 vcc, v11, v68
	s_and_saveexec_b64 s[32:33], vcc
	global_load_dword v8, v67, s[12:13] offset:92
	s_mov_b64 exec, s[32:33]
	s_waitcnt vmcnt(0)
	v_lshlrev_b32_e32 v5, 4, v5
	v_lshlrev_b32_e32 v6, 4, v6
	v_lshlrev_b32_e32 v7, 4, v7
	v_lshlrev_b32_e32 v8, 4, v8
	s_mov_b32 s42, 0
	s_mov_b32 s43, 0
	s_cmp_lt_i32 s29, 3
	s_cbranch_scc1 .Lagg_first_half
	ds_swizzle_b32 v32, v5 offset:swizzle(BITMASK_PERM, "pp000")
	ds_swizzle_b32 v33, v5 offset:swizzle(BITMASK_PERM, "pp001")
	ds_swizzle_b32 v34, v5 offset:swizzle(BITMASK_PERM, "pp010")
	ds_swizzle_b32 v35, v5 offset:swizzle(BITMASK_PERM, "pp011")
	s_waitcnt lgkmcnt(0)
	v_or_b32_e32 v32, v32, v1
	v_or_b32_e32 v33, v33, v1
	v_or_b32_e32 v34, v34, v1
	v_or_b32_e32 v35, v35, v1
	global_load_ushort v36, v32, s[6:7]
	global_load_ushort v37, v33, s[6:7]
	global_load_ushort v38, v34, s[6:7]
	global_load_ushort v39, v35, s[6:7]
	v_lshlrev_b32_e32 v32, 3, v32
	v_lshlrev_b32_e32 v33, 3, v33
	v_lshlrev_b32_e32 v34, 3, v34
	v_lshlrev_b32_e32 v35, 3, v35
	global_load_dwordx4 v[40:43], v32, s[4:5]
	global_load_dwordx4 v[44:47], v33, s[4:5]
	global_load_dwordx4 v[48:51], v34, s[4:5]
	global_load_dwordx4 v[52:55], v35, s[4:5]
	s_waitcnt vmcnt(4)
	v_fma_mix_f32 v36, v36, 1.0, v9 op_sel_hi:[1,0,0]
	v_fma_mix_f32 v37, v37, 1.0, v9 op_sel_hi:[1,0,0]
	v_fma_mix_f32 v38, v38, 1.0, v9 op_sel_hi:[1,0,0]
	v_fma_mix_f32 v39, v39, 1.0, v9 op_sel_hi:[1,0,0]
	v_mul_f32_e32 v58, 0x3e4ccccd, v36
	v_mul_f32_e32 v59, 0x3e4ccccd, v37
	v_mul_f32_e32 v60, 0x3e4ccccd, v38
	v_mul_f32_e32 v61, 0x3e4ccccd, v39
	v_max_f32_e32 v36, v36, v58
	v_max_f32_e32 v37, v37, v59
	v_max_f32_e32 v38, v38, v60
	v_max_f32_e32 v39, v39, v61
	v_max3_f32 v56, v36, v37, v38
	v_max_f32_e32 v13, v56, v39
	v_sub_f32_e32 v36, v36, v13
	v_sub_f32_e32 v37, v37, v13
	v_sub_f32_e32 v38, v38, v13
	v_sub_f32_e32 v39, v39, v13
	v_exp_f32_e32 v36, v36
	v_exp_f32_e32 v37, v37
	v_exp_f32_e32 v38, v38
	v_exp_f32_e32 v39, v39
	s_nop 0
	v_add_f32_e32 v14, v36, v37
	v_add_f32_e32 v14, v14, v38
	v_add_f32_e32 v14, v14, v39
	s_waitcnt vmcnt(3)
	v_cvt_scalef32_pk_f16_fp8 v58, v40, 1.0
	v_cvt_scalef32_pk_f16_fp8 v59, v40, 1.0 op_sel:[1,0,0]
	v_cvt_scalef32_pk_f16_fp8 v60, v41, 1.0
	v_cvt_scalef32_pk_f16_fp8 v61, v41, 1.0 op_sel:[1,0,0]
	v_fma_mix_f32 v16, v58, v36, 0 op_sel_hi:[1,0,0]
	v_fma_mix_f32 v17, v58, v36, 0 op_sel:[1,0,0] op_sel_hi:[1,0,0]
	v_fma_mix_f32 v18, v59, v36, 0 op_sel_hi:[1,0,0]
	v_fma_mix_f32 v19, v59, v36, 0 op_sel:[1,0,0] op_sel_hi:[1,0,0]
	v_fma_mix_f32 v20, v60, v36, 0 op_sel_hi:[1,0,0]
	v_fma_mix_f32 v21, v60, v36, 0 op_sel:[1,0,0] op_sel_hi:[1,0,0]
	v_fma_mix_f32 v22, v61, v36, 0 op_sel_hi:[1,0,0]
	v_fma_mix_f32 v23, v61, v36, 0 op_sel:[1,0,0] op_sel_hi:[1,0,0]
	v_cvt_scalef32_pk_f16_fp8 v58, v42, 1.0
	v_cvt_scalef32_pk_f16_fp8 v59, v42, 1.0 op_sel:[1,0,0]
	v_cvt_scalef32_pk_f16_fp8 v60, v43, 1.0
	v_cvt_scalef32_pk_f16_fp8 v61, v43, 1.0 op_sel:[1,0,0]
	v_fma_mix_f32 v24, v58, v36, 0 op_sel_hi:[1,0,0]
	v_fma_mix_f32 v25, v58, v36, 0 op_sel:[1,0,0] op_sel_hi:[1,0,0]
	v_fma_mix_f32 v26, v59, v36, 0 op_sel_hi:[1,0,0]
	v_fma_mix_f32 v27, v59, v36, 0 op_sel:[1,0,0] op_sel_hi:[1,0,0]
	v_fma_mix_f32 v28, v60, v36, 0 op_sel_hi:[1,0,0]
	v_fma_mix_f32 v29, v60, v36, 0 op_sel:[1,0,0] op_sel_hi:[1,0,0]
	v_fma_mix_f32 v30, v61, v36, 0 op_sel_hi:[1,0,0]
	v_fma_mix_f32 v31, v61, v36, 0 op_sel:[1,0,0] op_sel_hi:[1,0,0]
	s_waitcnt vmcnt(2)
	v_cvt_scalef32_pk_f16_fp8 v58, v44, 1.0
	v_cvt_scalef32_pk_f16_fp8 v59, v44, 1.0 op_sel:[1,0,0]
	v_cvt_scalef32_pk_f16_fp8 v60, v45, 1.0
	v_cvt_scalef32_pk_f16_fp8 v61, v45, 1.0 op_sel:[1,0,0]
	v_fma_mix_f32 v16, v58, v37, v16 op_sel_hi:[1,0,0]
	v_fma_mix_f32 v17, v58, v37, v17 op_sel:[1,0,0] op_sel_hi:[1,0,0]
	v_fma_mix_f32 v18, v59, v37, v18 op_sel_hi:[1,0,0]
	v_fma_mix_f32 v19, v59, v37, v19 op_sel:[1,0,0] op_sel_hi:[1,0,0]
	v_fma_mix_f32 v20, v60, v37, v20 op_sel_hi:[1,0,0]
	v_fma_mix_f32 v21, v60, v37, v21 op_sel:[1,0,0] op_sel_hi:[1,0,0]
	v_fma_mix_f32 v22, v61, v37, v22 op_sel_hi:[1,0,0]
	v_fma_mix_f32 v23, v61, v37, v23 op_sel:[1,0,0] op_sel_hi:[1,0,0]
	v_cvt_scalef32_pk_f16_fp8 v58, v46, 1.0
	v_cvt_scalef32_pk_f16_fp8 v59, v46, 1.0 op_sel:[1,0,0]
	v_cvt_scalef32_pk_f16_fp8 v60, v47, 1.0
	v_cvt_scalef32_pk_f16_fp8 v61, v47, 1.0 op_sel:[1,0,0]
	v_fma_mix_f32 v24, v58, v37, v24 op_sel_hi:[1,0,0]
	v_fma_mix_f32 v25, v58, v37, v25 op_sel:[1,0,0] op_sel_hi:[1,0,0]
	v_fma_mix_f32 v26, v59, v37, v26 op_sel_hi:[1,0,0]
	v_fma_mix_f32 v27, v59, v37, v27 op_sel:[1,0,0] op_sel_hi:[1,0,0]
	v_fma_mix_f32 v28, v60, v37, v28 op_sel_hi:[1,0,0]
	v_fma_mix_f32 v29, v60, v37, v29 op_sel:[1,0,0] op_sel_hi:[1,0,0]
	v_fma_mix_f32 v30, v61, v37, v30 op_sel_hi:[1,0,0]
	v_fma_mix_f32 v31, v61, v37, v31 op_sel:[1,0,0] op_sel_hi:[1,0,0]
	s_waitcnt vmcnt(1)
	v_cvt_scalef32_pk_f16_fp8 v58, v48, 1.0
	v_cvt_scalef32_pk_f16_fp8 v59, v48, 1.0 op_sel:[1,0,0]
	v_cvt_scalef32_pk_f16_fp8 v60, v49, 1.0
	v_cvt_scalef32_pk_f16_fp8 v61, v49, 1.0 op_sel:[1,0,0]
	v_fma_mix_f32 v16, v58, v38, v16 op_sel_hi:[1,0,0]
	v_fma_mix_f32 v17, v58, v38, v17 op_sel:[1,0,0] op_sel_hi:[1,0,0]
	v_fma_mix_f32 v18, v59, v38, v18 op_sel_hi:[1,0,0]
	v_fma_mix_f32 v19, v59, v38, v19 op_sel:[1,0,0] op_sel_hi:[1,0,0]
	v_fma_mix_f32 v20, v60, v38, v20 op_sel_hi:[1,0,0]
	v_fma_mix_f32 v21, v60, v38, v21 op_sel:[1,0,0] op_sel_hi:[1,0,0]
	v_fma_mix_f32 v22, v61, v38, v22 op_sel_hi:[1,0,0]
	v_fma_mix_f32 v23, v61, v38, v23 op_sel:[1,0,0] op_sel_hi:[1,0,0]
	v_cvt_scalef32_pk_f16_fp8 v58, v50, 1.0
	v_cvt_scalef32_pk_f16_fp8 v59, v50, 1.0 op_sel:[1,0,0]
	v_cvt_scalef32_pk_f16_fp8 v60, v51, 1.0
	v_cvt_scalef32_pk_f16_fp8 v61, v51, 1.0 op_sel:[1,0,0]
	v_fma_mix_f32 v24, v58, v38, v24 op_sel_hi:[1,0,0]
	v_fma_mix_f32 v25, v58, v38, v25 op_sel:[1,0,0] op_sel_hi:[1,0,0]
	v_fma_mix_f32 v26, v59, v38, v26 op_sel_hi:[1,0,0]
	v_fma_mix_f32 v27, v59, v38, v27 op_sel:[1,0,0] op_sel_hi:[1,0,0]
	v_fma_mix_f32 v28, v60, v38, v28 op_sel_hi:[1,0,0]
	v_fma_mix_f32 v29, v60, v38, v29 op_sel:[1,0,0] op_sel_hi:[1,0,0]
	v_fma_mix_f32 v30, v61, v38, v30 op_sel_hi:[1,0,0]
	v_fma_mix_f32 v31, v61, v38, v31 op_sel:[1,0,0] op_sel_hi:[1,0,0]
	s_waitcnt vmcnt(0)
	v_cvt_scalef32_pk_f16_fp8 v58, v52, 1.0
	v_cvt_scalef32_pk_f16_fp8 v59, v52, 1.0 op_sel:[1,0,0]
	v_cvt_scalef32_pk_f16_fp8 v60, v53, 1.0
	v_cvt_scalef32_pk_f16_fp8 v61, v53, 1.0 op_sel:[1,0,0]
	v_fma_mix_f32 v16, v58, v39, v16 op_sel_hi:[1,0,0]
	v_fma_mix_f32 v17, v58, v39, v17 op_sel:[1,0,0] op_sel_hi:[1,0,0]
	v_fma_mix_f32 v18, v59, v39, v18 op_sel_hi:[1,0,0]
	v_fma_mix_f32 v19, v59, v39, v19 op_sel:[1,0,0] op_sel_hi:[1,0,0]
	v_fma_mix_f32 v20, v60, v39, v20 op_sel_hi:[1,0,0]
	v_fma_mix_f32 v21, v60, v39, v21 op_sel:[1,0,0] op_sel_hi:[1,0,0]
	v_fma_mix_f32 v22, v61, v39, v22 op_sel_hi:[1,0,0]
	v_fma_mix_f32 v23, v61, v39, v23 op_sel:[1,0,0] op_sel_hi:[1,0,0]
	v_cvt_scalef32_pk_f16_fp8 v58, v54, 1.0
	v_cvt_scalef32_pk_f16_fp8 v59, v54, 1.0 op_sel:[1,0,0]
	v_cvt_scalef32_pk_f16_fp8 v60, v55, 1.0
	v_cvt_scalef32_pk_f16_fp8 v61, v55, 1.0 op_sel:[1,0,0]
	v_fma_mix_f32 v24, v58, v39, v24 op_sel_hi:[1,0,0]
	v_fma_mix_f32 v25, v58, v39, v25 op_sel:[1,0,0] op_sel_hi:[1,0,0]
	v_fma_mix_f32 v26, v59, v39, v26 op_sel_hi:[1,0,0]
	v_fma_mix_f32 v27, v59, v39, v27 op_sel:[1,0,0] op_sel_hi:[1,0,0]
	v_fma_mix_f32 v28, v60, v39, v28 op_sel_hi:[1,0,0]
	v_fma_mix_f32 v29, v60, v39, v29 op_sel:[1,0,0] op_sel_hi:[1,0,0]
	v_fma_mix_f32 v30, v61, v39, v30 op_sel_hi:[1,0,0]
	v_fma_mix_f32 v31, v61, v39, v31 op_sel:[1,0,0] op_sel_hi:[1,0,0]
	s_sub_i32 s29, s29, 4
	s_branch .Lagg_B
.Lagg_first_half:
	ds_swizzle_b32 v32, v5 offset:swizzle(BITMASK_PERM, "pp000")
	ds_swizzle_b32 v33, v5 offset:swizzle(BITMASK_PERM, "pp001")
	s_waitcnt lgkmcnt(0)
	v_or_b32_e32 v32, v32, v1
	v_or_b32_e32 v33, v33, v1
	global_load_ushort v36, v32, s[6:7]
	global_load_ushort v37, v33, s[6:7]
	v_lshlrev_b32_e32 v32, 3, v32
	v_lshlrev_b32_e32 v33, 3, v33
	global_load_dwordx4 v[40:43], v32, s[4:5]
	global_load_dwordx4 v[44:47], v33, s[4:5]
	s_waitcnt vmcnt(2)
	v_fma_mix_f32 v36, v36, 1.0, v9 op_sel_hi:[1,0,0]
	v_fma_mix_f32 v37, v37, 1.0, v9 op_sel_hi:[1,0,0]
	v_mul_f32_e32 v58, 0x3e4ccccd, v36
	v_mul_f32_e32 v59, 0x3e4ccccd, v37
	v_max_f32_e32 v36, v36, v58
	v_max_f32_e32 v37, v37, v59
	v_max_f32_e32 v13, v36, v37
	v_sub_f32_e32 v36, v36, v13
	v_sub_f32_e32 v37, v37, v13
	v_exp_f32_e32 v36, v36
	v_exp_f32_e32 v37, v37
	s_nop 0
	v_add_f32_e32 v14, v36, v37
	s_waitcnt vmcnt(1)
	v_cvt_scalef32_pk_f16_fp8 v58, v40, 1.0
	v_cvt_scalef32_pk_f16_fp8 v59, v40, 1.0 op_sel:[1,0,0]
	v_cvt_scalef32_pk_f16_fp8 v60, v41, 1.0
	v_cvt_scalef32_pk_f16_fp8 v61, v41, 1.0 op_sel:[1,0,0]
	v_fma_mix_f32 v16, v58, v36, 0 op_sel_hi:[1,0,0]
	v_fma_mix_f32 v17, v58, v36, 0 op_sel:[1,0,0] op_sel_hi:[1,0,0]
	v_fma_mix_f32 v18, v59, v36, 0 op_sel_hi:[1,0,0]
	v_fma_mix_f32 v19, v59, v36, 0 op_sel:[1,0,0] op_sel_hi:[1,0,0]
	v_fma_mix_f32 v20, v60, v36, 0 op_sel_hi:[1,0,0]
	v_fma_mix_f32 v21, v60, v36, 0 op_sel:[1,0,0] op_sel_hi:[1,0,0]
	v_fma_mix_f32 v22, v61, v36, 0 op_sel_hi:[1,0,0]
	v_fma_mix_f32 v23, v61, v36, 0 op_sel:[1,0,0] op_sel_hi:[1,0,0]
	v_cvt_scalef32_pk_f16_fp8 v58, v42, 1.0
	v_cvt_scalef32_pk_f16_fp8 v59, v42, 1.0 op_sel:[1,0,0]
	v_cvt_scalef32_pk_f16_fp8 v60, v43, 1.0
	v_cvt_scalef32_pk_f16_fp8 v61, v43, 1.0 op_sel:[1,0,0]
	v_fma_mix_f32 v24, v58, v36, 0 op_sel_hi:[1,0,0]
	v_fma_mix_f32 v25, v58, v36, 0 op_sel:[1,0,0] op_sel_hi:[1,0,0]
	v_fma_mix_f32 v26, v59, v36, 0 op_sel_hi:[1,0,0]
	v_fma_mix_f32 v27, v59, v36, 0 op_sel:[1,0,0] op_sel_hi:[1,0,0]
	v_fma_mix_f32 v28, v60, v36, 0 op_sel_hi:[1,0,0]
	v_fma_mix_f32 v29, v60, v36, 0 op_sel:[1,0,0] op_sel_hi:[1,0,0]
	v_fma_mix_f32 v30, v61, v36, 0 op_sel_hi:[1,0,0]
	v_fma_mix_f32 v31, v61, v36, 0 op_sel:[1,0,0] op_sel_hi:[1,0,0]
	s_waitcnt vmcnt(0)
	v_cvt_scalef32_pk_f16_fp8 v58, v44, 1.0
	v_cvt_scalef32_pk_f16_fp8 v59, v44, 1.0 op_sel:[1,0,0]
	v_cvt_scalef32_pk_f16_fp8 v60, v45, 1.0
	v_cvt_scalef32_pk_f16_fp8 v61, v45, 1.0 op_sel:[1,0,0]
	v_fma_mix_f32 v16, v58, v37, v16 op_sel_hi:[1,0,0]
	v_fma_mix_f32 v17, v58, v37, v17 op_sel:[1,0,0] op_sel_hi:[1,0,0]
	v_fma_mix_f32 v18, v59, v37, v18 op_sel_hi:[1,0,0]
	v_fma_mix_f32 v19, v59, v37, v19 op_sel:[1,0,0] op_sel_hi:[1,0,0]
	v_fma_mix_f32 v20, v60, v37, v20 op_sel_hi:[1,0,0]
	v_fma_mix_f32 v21, v60, v37, v21 op_sel:[1,0,0] op_sel_hi:[1,0,0]
	v_fma_mix_f32 v22, v61, v37, v22 op_sel_hi:[1,0,0]
	v_fma_mix_f32 v23, v61, v37, v23 op_sel:[1,0,0] op_sel_hi:[1,0,0]
	v_cvt_scalef32_pk_f16_fp8 v58, v46, 1.0
	v_cvt_scalef32_pk_f16_fp8 v59, v46, 1.0 op_sel:[1,0,0]
	v_cvt_scalef32_pk_f16_fp8 v60, v47, 1.0
	v_cvt_scalef32_pk_f16_fp8 v61, v47, 1.0 op_sel:[1,0,0]
	v_fma_mix_f32 v24, v58, v37, v24 op_sel_hi:[1,0,0]
	v_fma_mix_f32 v25, v58, v37, v25 op_sel:[1,0,0] op_sel_hi:[1,0,0]
	v_fma_mix_f32 v26, v59, v37, v26 op_sel_hi:[1,0,0]
	v_fma_mix_f32 v27, v59, v37, v27 op_sel:[1,0,0] op_sel_hi:[1,0,0]
	v_fma_mix_f32 v28, v60, v37, v28 op_sel_hi:[1,0,0]
	v_fma_mix_f32 v29, v60, v37, v29 op_sel:[1,0,0] op_sel_hi:[1,0,0]
	v_fma_mix_f32 v30, v61, v37, v30 op_sel_hi:[1,0,0]
	v_fma_mix_f32 v31, v61, v37, v31 op_sel:[1,0,0] op_sel_hi:[1,0,0]
	s_branch .Lagg_epi
.Lagg_B:
	s_cmp_lt_i32 s29, 1
	s_cbranch_scc1 .Lagg_epi
	s_cmp_lt_i32 s29, 3
	s_cbranch_scc1 .Lagg_B_half
	ds_swizzle_b32 v32, v5 offset:swizzle(BITMASK_PERM, "pp100")
	ds_swizzle_b32 v33, v5 offset:swizzle(BITMASK_PERM, "pp101")
	ds_swizzle_b32 v34, v5 offset:swizzle(BITMASK_PERM, "pp110")
	ds_swizzle_b32 v35, v5 offset:swizzle(BITMASK_PERM, "pp111")
	s_waitcnt lgkmcnt(0)
	v_or_b32_e32 v32, v32, v1
	v_or_b32_e32 v33, v33, v1
	v_or_b32_e32 v34, v34, v1
	v_or_b32_e32 v35, v35, v1
	global_load_ushort v36, v32, s[6:7]
	global_load_ushort v37, v33, s[6:7]
	global_load_ushort v38, v34, s[6:7]
	global_load_ushort v39, v35, s[6:7]
	v_lshlrev_b32_e32 v32, 3, v32
	v_lshlrev_b32_e32 v33, 3, v33
	v_lshlrev_b32_e32 v34, 3, v34
	v_lshlrev_b32_e32 v35, 3, v35
	global_load_dwordx4 v[40:43], v32, s[4:5]
	global_load_dwordx4 v[44:47], v33, s[4:5]
	global_load_dwordx4 v[48:51], v34, s[4:5]
	global_load_dwordx4 v[52:55], v35, s[4:5]
	s_waitcnt vmcnt(4)
	v_fma_mix_f32 v36, v36, 1.0, v9 op_sel_hi:[1,0,0]
	v_fma_mix_f32 v37, v37, 1.0, v9 op_sel_hi:[1,0,0]
	v_fma_mix_f32 v38, v38, 1.0, v9 op_sel_hi:[1,0,0]
	v_fma_mix_f32 v39, v39, 1.0, v9 op_sel_hi:[1,0,0]
	v_mul_f32_e32 v58, 0x3e4ccccd, v36
	v_mul_f32_e32 v59, 0x3e4ccccd, v37
	v_mul_f32_e32 v60, 0x3e4ccccd, v38
	v_mul_f32_e32 v61, 0x3e4ccccd, v39
	v_max_f32_e32 v36, v36, v58
	v_max_f32_e32 v37, v37, v59
	v_max_f32_e32 v38, v38, v60
	v_max_f32_e32 v39, v39, v61
	v_max3_f32 v56, v13, v36, v37
	v_max3_f32 v12, v56, v38, v39
	v_sub_f32_e32 v57, v13, v12
	v_sub_f32_e32 v36, v36, v12
	v_sub_f32_e32 v37, v37, v12
	v_sub_f32_e32 v38, v38, v12
	v_sub_f32_e32 v39, v39, v12
	v_exp_f32_e32 v57, v57
	v_exp_f32_e32 v36, v36
	v_exp_f32_e32 v37, v37
	v_exp_f32_e32 v38, v38
	v_exp_f32_e32 v39, v39
	v_fma_f32 v14, v14, v57, v36
	v_mul_f32_e32 v16, v16, v57
	v_mul_f32_e32 v17, v17, v57
	v_mul_f32_e32 v18, v18, v57
	v_mul_f32_e32 v19, v19, v57
	v_mul_f32_e32 v20, v20, v57
	v_mul_f32_e32 v21, v21, v57
	v_mul_f32_e32 v22, v22, v57
	v_mul_f32_e32 v23, v23, v57
	v_mul_f32_e32 v24, v24, v57
	v_mul_f32_e32 v25, v25, v57
	v_mul_f32_e32 v26, v26, v57
	v_mul_f32_e32 v27, v27, v57
	v_mul_f32_e32 v28, v28, v57
	v_mul_f32_e32 v29, v29, v57
	v_mul_f32_e32 v30, v30, v57
	v_mul_f32_e32 v31, v31, v57
	v_add_f32_e32 v14, v14, v37
	v_add_f32_e32 v14, v14, v38
	v_add_f32_e32 v14, v14, v39
	s_waitcnt vmcnt(3)
	v_cvt_scalef32_pk_f16_fp8 v58, v40, 1.0
	v_cvt_scalef32_pk_f16_fp8 v59, v40, 1.0 op_sel:[1,0,0]
	v_cvt_scalef32_pk_f16_fp8 v60, v41, 1.0
	v_cvt_scalef32_pk_f16_fp8 v61, v41, 1.0 op_sel:[1,0,0]
	v_fma_mix_f32 v16, v58, v36, v16 op_sel_hi:[1,0,0]
	v_fma_mix_f32 v17, v58, v36, v17 op_sel:[1,0,0] op_sel_hi:[1,0,0]
	v_fma_mix_f32 v18, v59, v36, v18 op_sel_hi:[1,0,0]
	v_fma_mix_f32 v19, v59, v36, v19 op_sel:[1,0,0] op_sel_hi:[1,0,0]
	v_fma_mix_f32 v20, v60, v36, v20 op_sel_hi:[1,0,0]
	v_fma_mix_f32 v21, v60, v36, v21 op_sel:[1,0,0] op_sel_hi:[1,0,0]
	v_fma_mix_f32 v22, v61, v36, v22 op_sel_hi:[1,0,0]
	v_fma_mix_f32 v23, v61, v36, v23 op_sel:[1,0,0] op_sel_hi:[1,0,0]
	v_cvt_scalef32_pk_f16_fp8 v58, v42, 1.0
	v_cvt_scalef32_pk_f16_fp8 v59, v42, 1.0 op_sel:[1,0,0]
	v_cvt_scalef32_pk_f16_fp8 v60, v43, 1.0
	v_cvt_scalef32_pk_f16_fp8 v61, v43, 1.0 op_sel:[1,0,0]
	v_fma_mix_f32 v24, v58, v36, v24 op_sel_hi:[1,0,0]
	v_fma_mix_f32 v25, v58, v36, v25 op_sel:[1,0,0] op_sel_hi:[1,0,0]
	v_fma_mix_f32 v26, v59, v36, v26 op_sel_hi:[1,0,0]
	v_fma_mix_f32 v27, v59, v36, v27 op_sel:[1,0,0] op_sel_hi:[1,0,0]
	v_fma_mix_f32 v28, v60, v36, v28 op_sel_hi:[1,0,0]
	v_fma_mix_f32 v29, v60, v36, v29 op_sel:[1,0,0] op_sel_hi:[1,0,0]
	v_fma_mix_f32 v30, v61, v36, v30 op_sel_hi:[1,0,0]
	v_fma_mix_f32 v31, v61, v36, v31 op_sel:[1,0,0] op_sel_hi:[1,0,0]
	s_waitcnt vmcnt(2)
	v_cvt_scalef32_pk_f16_fp8 v58, v44, 1.0
	v_cvt_scalef32_pk_f16_fp8 v59, v44, 1.0 op_sel:[1,0,0]
	v_cvt_scalef32_pk_f16_fp8 v60, v45, 1.0
	v_cvt_scalef32_pk_f16_fp8 v61, v45, 1.0 op_sel:[1,0,0]
	v_fma_mix_f32 v16, v58, v37, v16 op_sel_hi:[1,0,0]
	v_fma_mix_f32 v17, v58, v37, v17 op_sel:[1,0,0] op_sel_hi:[1,0,0]
	v_fma_mix_f32 v18, v59, v37, v18 op_sel_hi:[1,0,0]
	v_fma_mix_f32 v19, v59, v37, v19 op_sel:[1,0,0] op_sel_hi:[1,0,0]
	v_fma_mix_f32 v20, v60, v37, v20 op_sel_hi:[1,0,0]
	v_fma_mix_f32 v21, v60, v37, v21 op_sel:[1,0,0] op_sel_hi:[1,0,0]
	v_fma_mix_f32 v22, v61, v37, v22 op_sel_hi:[1,0,0]
	v_fma_mix_f32 v23, v61, v37, v23 op_sel:[1,0,0] op_sel_hi:[1,0,0]
	v_cvt_scalef32_pk_f16_fp8 v58, v46, 1.0
	v_cvt_scalef32_pk_f16_fp8 v59, v46, 1.0 op_sel:[1,0,0]
	v_cvt_scalef32_pk_f16_fp8 v60, v47, 1.0
	v_cvt_scalef32_pk_f16_fp8 v61, v47, 1.0 op_sel:[1,0,0]
	v_fma_mix_f32 v24, v58, v37, v24 op_sel_hi:[1,0,0]
	v_fma_mix_f32 v25, v58, v37, v25 op_sel:[1,0,0] op_sel_hi:[1,0,0]
	v_fma_mix_f32 v26, v59, v37, v26 op_sel_hi:[1,0,0]
	v_fma_mix_f32 v27, v59, v37, v27 op_sel:[1,0,0] op_sel_hi:[1,0,0]
	v_fma_mix_f32 v28, v60, v37, v28 op_sel_hi:[1,0,0]
	v_fma_mix_f32 v29, v60, v37, v29 op_sel:[1,0,0] op_sel_hi:[1,0,0]
	v_fma_mix_f32 v30, v61, v37, v30 op_sel_hi:[1,0,0]
	v_fma_mix_f32 v31, v61, v37, v31 op_sel:[1,0,0] op_sel_hi:[1,0,0]
	s_waitcnt vmcnt(1)
	v_cvt_scalef32_pk_f16_fp8 v58, v48, 1.0
	v_cvt_scalef32_pk_f16_fp8 v59, v48, 1.0 op_sel:[1,0,0]
	v_cvt_scalef32_pk_f16_fp8 v60, v49, 1.0
	v_cvt_scalef32_pk_f16_fp8 v61, v49, 1.0 op_sel:[1,0,0]
	v_fma_mix_f32 v16, v58, v38, v16 op_sel_hi:[1,0,0]
	v_fma_mix_f32 v17, v58, v38, v17 op_sel:[1,0,0] op_sel_hi:[1,0,0]
	v_fma_mix_f32 v18, v59, v38, v18 op_sel_hi:[1,0,0]
	v_fma_mix_f32 v19, v59, v38, v19 op_sel:[1,0,0] op_sel_hi:[1,0,0]
	v_fma_mix_f32 v20, v60, v38, v20 op_sel_hi:[1,0,0]
	v_fma_mix_f32 v21, v60, v38, v21 op_sel:[1,0,0] op_sel_hi:[1,0,0]
	v_fma_mix_f32 v22, v61, v38, v22 op_sel_hi:[1,0,0]
	v_fma_mix_f32 v23, v61, v38, v23 op_sel:[1,0,0] op_sel_hi:[1,0,0]
	v_cvt_scalef32_pk_f16_fp8 v58, v50, 1.0
	v_cvt_scalef32_pk_f16_fp8 v59, v50, 1.0 op_sel:[1,0,0]
	v_cvt_scalef32_pk_f16_fp8 v60, v51, 1.0
	v_cvt_scalef32_pk_f16_fp8 v61, v51, 1.0 op_sel:[1,0,0]
	v_fma_mix_f32 v24, v58, v38, v24 op_sel_hi:[1,0,0]
	v_fma_mix_f32 v25, v58, v38, v25 op_sel:[1,0,0] op_sel_hi:[1,0,0]
	v_fma_mix_f32 v26, v59, v38, v26 op_sel_hi:[1,0,0]
	v_fma_mix_f32 v27, v59, v38, v27 op_sel:[1,0,0] op_sel_hi:[1,0,0]
	v_fma_mix_f32 v28, v60, v38, v28 op_sel_hi:[1,0,0]
	v_fma_mix_f32 v29, v60, v38, v29 op_sel:[1,0,0] op_sel_hi:[1,0,0]
	v_fma_mix_f32 v30, v61, v38, v30 op_sel_hi:[1,0,0]
	v_fma_mix_f32 v31, v61, v38, v31 op_sel:[1,0,0] op_sel_hi:[1,0,0]
	s_waitcnt vmcnt(0)
	v_cvt_scalef32_pk_f16_fp8 v58, v52, 1.0
	v_cvt_scalef32_pk_f16_fp8 v59, v52, 1.0 op_sel:[1,0,0]
	v_cvt_scalef32_pk_f16_fp8 v60, v53, 1.0
	v_cvt_scalef32_pk_f16_fp8 v61, v53, 1.0 op_sel:[1,0,0]
	v_fma_mix_f32 v16, v58, v39, v16 op_sel_hi:[1,0,0]
	v_fma_mix_f32 v17, v58, v39, v17 op_sel:[1,0,0] op_sel_hi:[1,0,0]
	v_fma_mix_f32 v18, v59, v39, v18 op_sel_hi:[1,0,0]
	v_fma_mix_f32 v19, v59, v39, v19 op_sel:[1,0,0] op_sel_hi:[1,0,0]
	v_fma_mix_f32 v20, v60, v39, v20 op_sel_hi:[1,0,0]
	v_fma_mix_f32 v21, v60, v39, v21 op_sel:[1,0,0] op_sel_hi:[1,0,0]
	v_fma_mix_f32 v22, v61, v39, v22 op_sel_hi:[1,0,0]
	v_fma_mix_f32 v23, v61, v39, v23 op_sel:[1,0,0] op_sel_hi:[1,0,0]
	v_cvt_scalef32_pk_f16_fp8 v58, v54, 1.0
	v_cvt_scalef32_pk_f16_fp8 v59, v54, 1.0 op_sel:[1,0,0]
	v_cvt_scalef32_pk_f16_fp8 v60, v55, 1.0
	v_cvt_scalef32_pk_f16_fp8 v61, v55, 1.0 op_sel:[1,0,0]
	v_fma_mix_f32 v24, v58, v39, v24 op_sel_hi:[1,0,0]
	v_fma_mix_f32 v25, v58, v39, v25 op_sel:[1,0,0] op_sel_hi:[1,0,0]
	v_fma_mix_f32 v26, v59, v39, v26 op_sel_hi:[1,0,0]
	v_fma_mix_f32 v27, v59, v39, v27 op_sel:[1,0,0] op_sel_hi:[1,0,0]
	v_fma_mix_f32 v28, v60, v39, v28 op_sel_hi:[1,0,0]
	v_fma_mix_f32 v29, v60, v39, v29 op_sel:[1,0,0] op_sel_hi:[1,0,0]
	v_fma_mix_f32 v30, v61, v39, v30 op_sel_hi:[1,0,0]
	v_fma_mix_f32 v31, v61, v39, v31 op_sel:[1,0,0] op_sel_hi:[1,0,0]
	s_sub_i32 s29, s29, 4
	v_mov_b32_e32 v5, v6
	v_mov_b32_e32 v6, v7
	v_mov_b32_e32 v7, v8
	s_add_i32 s43, s43, 1
	s_cmp_lt_i32 s29, 1
	s_cbranch_scc1 .Lagg_epi
	s_cmp_lg_u32 s43, 4
	s_cbranch_scc1 .Lagg_A
	s_add_i32 s42, s42, 32
	s_mov_b32 s43, 0
	v_add_u32_e32 v68, s42, v64
	v_add_u32_e32 v67, v10, v68
	v_lshlrev_b32_e32 v67, 2, v67
	v_mov_b32_e32 v5, s24
	v_mov_b32_e32 v6, s24
	v_mov_b32_e32 v7, s24
	v_mov_b32_e32 v8, s24
	v_cmp_gt_i32_e32 vcc, v11, v68
	s_and_saveexec_b64 s[32:33], vcc
	global_load_dword v5, v67, s[12:13] offset:-4
	s_mov_b64 exec, s[32:33]
	v_add_u32_e32 v68, 8, v68
	v_cmp_gt_i32_e32 vcc, v11, v68
	s_and_saveexec_b64 s[32:33], vcc
	global_load_dword v6, v67, s[12:13] offset:28
	s_mov_b64 exec, s[32:33]
	v_add_u32_e32 v68, 8, v68
	v_cmp_gt_i32_e32 vcc, v11, v68
	s_and_saveexec_b64 s[32:33], vcc
	global_load_dword v7, v67, s[12:13] offset:60
	s_mov_b64 exec, s[32:33]
	v_add_u32_e32 v68, 8, v68
	v_cmp_gt_i32_e32 vcc, v11, v68
	s_and_saveexec_b64 s[32:33], vcc
	global_load_dword v8, v67, s[12:13] offset:92
	s_mov_b64 exec, s[32:33]
	s_waitcnt vmcnt(0)
	v_lshlrev_b32_e32 v5, 4, v5
	v_lshlrev_b32_e32 v6, 4, v6
	v_lshlrev_b32_e32 v7, 4, v7
	v_lshlrev_b32_e32 v8, 4, v8
.Lagg_A:
	s_cmp_lt_i32 s29, 3
	s_cbranch_scc1 .Lagg_A_half
	ds_swizzle_b32 v32, v5 offset:swizzle(BITMASK_PERM, "pp000")
	ds_swizzle_b32 v33, v5 offset:swizzle(BITMASK_PERM, "pp001")
	ds_swizzle_b32 v34, v5 offset:swizzle(BITMASK_PERM, "pp010")
	ds_swizzle_b32 v35, v5 offset:swizzle(BITMASK_PERM, "pp011")
	s_waitcnt lgkmcnt(0)
	v_or_b32_e32 v32, v32, v1
	v_or_b32_e32 v33, v33, v1
	v_or_b32_e32 v34, v34, v1
	v_or_b32_e32 v35, v35, v1
	global_load_ushort v36, v32, s[6:7]
	global_load_ushort v37, v33, s[6:7]
	global_load_ushort v38, v34, s[6:7]
	global_load_ushort v39, v35, s[6:7]
	v_lshlrev_b32_e32 v32, 3, v32
	v_lshlrev_b32_e32 v33, 3, v33
	v_lshlrev_b32_e32 v34, 3, v34
	v_lshlrev_b32_e32 v35, 3, v35
	global_load_dwordx4 v[40:43], v32, s[4:5]
	global_load_dwordx4 v[44:47], v33, s[4:5]
	global_load_dwordx4 v[48:51], v34, s[4:5]
	global_load_dwordx4 v[52:55], v35, s[4:5]
	s_waitcnt vmcnt(4)
	v_fma_mix_f32 v36, v36, 1.0, v9 op_sel_hi:[1,0,0]
	v_fma_mix_f32 v37, v37, 1.0, v9 op_sel_hi:[1,0,0]
	v_fma_mix_f32 v38, v38, 1.0, v9 op_sel_hi:[1,0,0]
	v_fma_mix_f32 v39, v39, 1.0, v9 op_sel_hi:[1,0,0]
	v_mul_f32_e32 v58, 0x3e4ccccd, v36
	v_mul_f32_e32 v59, 0x3e4ccccd, v37
	v_mul_f32_e32 v60, 0x3e4ccccd, v38
	v_mul_f32_e32 v61, 0x3e4ccccd, v39
	v_max_f32_e32 v36, v36, v58
	v_max_f32_e32 v37, v37, v59
	v_max_f32_e32 v38, v38, v60
	v_max_f32_e32 v39, v39, v61
	v_max3_f32 v56, v12, v36, v37
	v_max3_f32 v13, v56, v38, v39
	v_sub_f32_e32 v57, v12, v13
	v_sub_f32_e32 v36, v36, v13
	v_sub_f32_e32 v37, v37, v13
	v_sub_f32_e32 v38, v38, v13
	v_sub_f32_e32 v39, v39, v13
	v_exp_f32_e32 v57, v57
	v_exp_f32_e32 v36, v36
	v_exp_f32_e32 v37, v37
	v_exp_f32_e32 v38, v38
	v_exp_f32_e32 v39, v39
	v_fma_f32 v14, v14, v57, v36
	v_mul_f32_e32 v16, v16, v57
	v_mul_f32_e32 v17, v17, v57
	v_mul_f32_e32 v18, v18, v57
	v_mul_f32_e32 v19, v19, v57
	v_mul_f32_e32 v20, v20, v57
	v_mul_f32_e32 v21, v21, v57
	v_mul_f32_e32 v22, v22, v57
	v_mul_f32_e32 v23, v23, v57
	v_mul_f32_e32 v24, v24, v57
	v_mul_f32_e32 v25, v25, v57
	v_mul_f32_e32 v26, v26, v57
	v_mul_f32_e32 v27, v27, v57
	v_mul_f32_e32 v28, v28, v57
	v_mul_f32_e32 v29, v29, v57
	v_mul_f32_e32 v30, v30, v57
	v_mul_f32_e32 v31, v31, v57
	v_add_f32_e32 v14, v14, v37
	v_add_f32_e32 v14, v14, v38
	v_add_f32_e32 v14, v14, v39
	s_waitcnt vmcnt(3)
	v_cvt_scalef32_pk_f16_fp8 v58, v40, 1.0
	v_cvt_scalef32_pk_f16_fp8 v59, v40, 1.0 op_sel:[1,0,0]
	v_cvt_scalef32_pk_f16_fp8 v60, v41, 1.0
	v_cvt_scalef32_pk_f16_fp8 v61, v41, 1.0 op_sel:[1,0,0]
	v_fma_mix_f32 v16, v58, v36, v16 op_sel_hi:[1,0,0]
	v_fma_mix_f32 v17, v58, v36, v17 op_sel:[1,0,0] op_sel_hi:[1,0,0]
	v_fma_mix_f32 v18, v59, v36, v18 op_sel_hi:[1,0,0]
	v_fma_mix_f32 v19, v59, v36, v19 op_sel:[1,0,0] op_sel_hi:[1,0,0]
	v_fma_mix_f32 v20, v60, v36, v20 op_sel_hi:[1,0,0]
	v_fma_mix_f32 v21, v60, v36, v21 op_sel:[1,0,0] op_sel_hi:[1,0,0]
	v_fma_mix_f32 v22, v61, v36, v22 op_sel_hi:[1,0,0]
	v_fma_mix_f32 v23, v61, v36, v23 op_sel:[1,0,0] op_sel_hi:[1,0,0]
	v_cvt_scalef32_pk_f16_fp8 v58, v42, 1.0
	v_cvt_scalef32_pk_f16_fp8 v59, v42, 1.0 op_sel:[1,0,0]
	v_cvt_scalef32_pk_f16_fp8 v60, v43, 1.0
	v_cvt_scalef32_pk_f16_fp8 v61, v43, 1.0 op_sel:[1,0,0]
	v_fma_mix_f32 v24, v58, v36, v24 op_sel_hi:[1,0,0]
	v_fma_mix_f32 v25, v58, v36, v25 op_sel:[1,0,0] op_sel_hi:[1,0,0]
	v_fma_mix_f32 v26, v59, v36, v26 op_sel_hi:[1,0,0]
	v_fma_mix_f32 v27, v59, v36, v27 op_sel:[1,0,0] op_sel_hi:[1,0,0]
	v_fma_mix_f32 v28, v60, v36, v28 op_sel_hi:[1,0,0]
	v_fma_mix_f32 v29, v60, v36, v29 op_sel:[1,0,0] op_sel_hi:[1,0,0]
	v_fma_mix_f32 v30, v61, v36, v30 op_sel_hi:[1,0,0]
	v_fma_mix_f32 v31, v61, v36, v31 op_sel:[1,0,0] op_sel_hi:[1,0,0]
	s_waitcnt vmcnt(2)
	v_cvt_scalef32_pk_f16_fp8 v58, v44, 1.0
	v_cvt_scalef32_pk_f16_fp8 v59, v44, 1.0 op_sel:[1,0,0]
	v_cvt_scalef32_pk_f16_fp8 v60, v45, 1.0
	v_cvt_scalef32_pk_f16_fp8 v61, v45, 1.0 op_sel:[1,0,0]
	v_fma_mix_f32 v16, v58, v37, v16 op_sel_hi:[1,0,0]
	v_fma_mix_f32 v17, v58, v37, v17 op_sel:[1,0,0] op_sel_hi:[1,0,0]
	v_fma_mix_f32 v18, v59, v37, v18 op_sel_hi:[1,0,0]
	v_fma_mix_f32 v19, v59, v37, v19 op_sel:[1,0,0] op_sel_hi:[1,0,0]
	v_fma_mix_f32 v20, v60, v37, v20 op_sel_hi:[1,0,0]
	v_fma_mix_f32 v21, v60, v37, v21 op_sel:[1,0,0] op_sel_hi:[1,0,0]
	v_fma_mix_f32 v22, v61, v37, v22 op_sel_hi:[1,0,0]
	v_fma_mix_f32 v23, v61, v37, v23 op_sel:[1,0,0] op_sel_hi:[1,0,0]
	v_cvt_scalef32_pk_f16_fp8 v58, v46, 1.0
	v_cvt_scalef32_pk_f16_fp8 v59, v46, 1.0 op_sel:[1,0,0]
	v_cvt_scalef32_pk_f16_fp8 v60, v47, 1.0
	v_cvt_scalef32_pk_f16_fp8 v61, v47, 1.0 op_sel:[1,0,0]
	v_fma_mix_f32 v24, v58, v37, v24 op_sel_hi:[1,0,0]
	v_fma_mix_f32 v25, v58, v37, v25 op_sel:[1,0,0] op_sel_hi:[1,0,0]
	v_fma_mix_f32 v26, v59, v37, v26 op_sel_hi:[1,0,0]
	v_fma_mix_f32 v27, v59, v37, v27 op_sel:[1,0,0] op_sel_hi:[1,0,0]
	v_fma_mix_f32 v28, v60, v37, v28 op_sel_hi:[1,0,0]
	v_fma_mix_f32 v29, v60, v37, v29 op_sel:[1,0,0] op_sel_hi:[1,0,0]
	v_fma_mix_f32 v30, v61, v37, v30 op_sel_hi:[1,0,0]
	v_fma_mix_f32 v31, v61, v37, v31 op_sel:[1,0,0] op_sel_hi:[1,0,0]
	s_waitcnt vmcnt(1)
	v_cvt_scalef32_pk_f16_fp8 v58, v48, 1.0
	v_cvt_scalef32_pk_f16_fp8 v59, v48, 1.0 op_sel:[1,0,0]
	v_cvt_scalef32_pk_f16_fp8 v60, v49, 1.0
	v_cvt_scalef32_pk_f16_fp8 v61, v49, 1.0 op_sel:[1,0,0]
	v_fma_mix_f32 v16, v58, v38, v16 op_sel_hi:[1,0,0]
	v_fma_mix_f32 v17, v58, v38, v17 op_sel:[1,0,0] op_sel_hi:[1,0,0]
	v_fma_mix_f32 v18, v59, v38, v18 op_sel_hi:[1,0,0]
	v_fma_mix_f32 v19, v59, v38, v19 op_sel:[1,0,0] op_sel_hi:[1,0,0]
	v_fma_mix_f32 v20, v60, v38, v20 op_sel_hi:[1,0,0]
	v_fma_mix_f32 v21, v60, v38, v21 op_sel:[1,0,0] op_sel_hi:[1,0,0]
	v_fma_mix_f32 v22, v61, v38, v22 op_sel_hi:[1,0,0]
	v_fma_mix_f32 v23, v61, v38, v23 op_sel:[1,0,0] op_sel_hi:[1,0,0]
	v_cvt_scalef32_pk_f16_fp8 v58, v50, 1.0
	v_cvt_scalef32_pk_f16_fp8 v59, v50, 1.0 op_sel:[1,0,0]
	v_cvt_scalef32_pk_f16_fp8 v60, v51, 1.0
	v_cvt_scalef32_pk_f16_fp8 v61, v51, 1.0 op_sel:[1,0,0]
	v_fma_mix_f32 v24, v58, v38, v24 op_sel_hi:[1,0,0]
	v_fma_mix_f32 v25, v58, v38, v25 op_sel:[1,0,0] op_sel_hi:[1,0,0]
	v_fma_mix_f32 v26, v59, v38, v26 op_sel_hi:[1,0,0]
	v_fma_mix_f32 v27, v59, v38, v27 op_sel:[1,0,0] op_sel_hi:[1,0,0]
	v_fma_mix_f32 v28, v60, v38, v28 op_sel_hi:[1,0,0]
	v_fma_mix_f32 v29, v60, v38, v29 op_sel:[1,0,0] op_sel_hi:[1,0,0]
	v_fma_mix_f32 v30, v61, v38, v30 op_sel_hi:[1,0,0]
	v_fma_mix_f32 v31, v61, v38, v31 op_sel:[1,0,0] op_sel_hi:[1,0,0]
	s_waitcnt vmcnt(0)
	v_cvt_scalef32_pk_f16_fp8 v58, v52, 1.0
	v_cvt_scalef32_pk_f16_fp8 v59, v52, 1.0 op_sel:[1,0,0]
	v_cvt_scalef32_pk_f16_fp8 v60, v53, 1.0
	v_cvt_scalef32_pk_f16_fp8 v61, v53, 1.0 op_sel:[1,0,0]
	v_fma_mix_f32 v16, v58, v39, v16 op_sel_hi:[1,0,0]
	v_fma_mix_f32 v17, v58, v39, v17 op_sel:[1,0,0] op_sel_hi:[1,0,0]
	v_fma_mix_f32 v18, v59, v39, v18 op_sel_hi:[1,0,0]
	v_fma_mix_f32 v19, v59, v39, v19 op_sel:[1,0,0] op_sel_hi:[1,0,0]
	v_fma_mix_f32 v20, v60, v39, v20 op_sel_hi:[1,0,0]
	v_fma_mix_f32 v21, v60, v39, v21 op_sel:[1,0,0] op_sel_hi:[1,0,0]
	v_fma_mix_f32 v22, v61, v39, v22 op_sel_hi:[1,0,0]
	v_fma_mix_f32 v23, v61, v39, v23 op_sel:[1,0,0] op_sel_hi:[1,0,0]
	v_cvt_scalef32_pk_f16_fp8 v58, v54, 1.0
	v_cvt_scalef32_pk_f16_fp8 v59, v54, 1.0 op_sel:[1,0,0]
	v_cvt_scalef32_pk_f16_fp8 v60, v55, 1.0
	v_cvt_scalef32_pk_f16_fp8 v61, v55, 1.0 op_sel:[1,0,0]
	v_fma_mix_f32 v24, v58, v39, v24 op_sel_hi:[1,0,0]
	v_fma_mix_f32 v25, v58, v39, v25 op_sel:[1,0,0] op_sel_hi:[1,0,0]
	v_fma_mix_f32 v26, v59, v39, v26 op_sel_hi:[1,0,0]
	v_fma_mix_f32 v27, v59, v39, v27 op_sel:[1,0,0] op_sel_hi:[1,0,0]
	v_fma_mix_f32 v28, v60, v39, v28 op_sel_hi:[1,0,0]
	v_fma_mix_f32 v29, v60, v39, v29 op_sel:[1,0,0] op_sel_hi:[1,0,0]
	v_fma_mix_f32 v30, v61, v39, v30 op_sel_hi:[1,0,0]
	v_fma_mix_f32 v31, v61, v39, v31 op_sel:[1,0,0] op_sel_hi:[1,0,0]
	s_sub_i32 s29, s29, 4
	s_branch .Lagg_B
.Lagg_A_half:
	ds_swizzle_b32 v32, v5 offset:swizzle(BITMASK_PERM, "pp000")
	ds_swizzle_b32 v33, v5 offset:swizzle(BITMASK_PERM, "pp001")
	s_waitcnt lgkmcnt(0)
	v_or_b32_e32 v32, v32, v1
	v_or_b32_e32 v33, v33, v1
	global_load_ushort v36, v32, s[6:7]
	global_load_ushort v37, v33, s[6:7]
	v_lshlrev_b32_e32 v32, 3, v32
	v_lshlrev_b32_e32 v33, 3, v33
	global_load_dwordx4 v[40:43], v32, s[4:5]
	global_load_dwordx4 v[44:47], v33, s[4:5]
	s_waitcnt vmcnt(2)
	v_fma_mix_f32 v36, v36, 1.0, v9 op_sel_hi:[1,0,0]
	v_fma_mix_f32 v37, v37, 1.0, v9 op_sel_hi:[1,0,0]
	v_mul_f32_e32 v58, 0x3e4ccccd, v36
	v_mul_f32_e32 v59, 0x3e4ccccd, v37
	v_max_f32_e32 v36, v36, v58
	v_max_f32_e32 v37, v37, v59
	v_max3_f32 v13, v12, v36, v37
	v_sub_f32_e32 v57, v12, v13
	v_sub_f32_e32 v36, v36, v13
	v_sub_f32_e32 v37, v37, v13
	v_exp_f32_e32 v57, v57
	v_exp_f32_e32 v36, v36
	v_exp_f32_e32 v37, v37
	v_fma_f32 v14, v14, v57, v36
	v_mul_f32_e32 v16, v16, v57
	v_mul_f32_e32 v17, v17, v57
	v_mul_f32_e32 v18, v18, v57
	v_mul_f32_e32 v19, v19, v57
	v_mul_f32_e32 v20, v20, v57
	v_mul_f32_e32 v21, v21, v57
	v_mul_f32_e32 v22, v22, v57
	v_mul_f32_e32 v23, v23, v57
	v_mul_f32_e32 v24, v24, v57
	v_mul_f32_e32 v25, v25, v57
	v_mul_f32_e32 v26, v26, v57
	v_mul_f32_e32 v27, v27, v57
	v_mul_f32_e32 v28, v28, v57
	v_mul_f32_e32 v29, v29, v57
	v_mul_f32_e32 v30, v30, v57
	v_mul_f32_e32 v31, v31, v57
	v_add_f32_e32 v14, v14, v37
	s_waitcnt vmcnt(1)
	v_cvt_scalef32_pk_f16_fp8 v58, v40, 1.0
	v_cvt_scalef32_pk_f16_fp8 v59, v40, 1.0 op_sel:[1,0,0]
	v_cvt_scalef32_pk_f16_fp8 v60, v41, 1.0
	v_cvt_scalef32_pk_f16_fp8 v61, v41, 1.0 op_sel:[1,0,0]
	v_fma_mix_f32 v16, v58, v36, v16 op_sel_hi:[1,0,0]
	v_fma_mix_f32 v17, v58, v36, v17 op_sel:[1,0,0] op_sel_hi:[1,0,0]
	v_fma_mix_f32 v18, v59, v36, v18 op_sel_hi:[1,0,0]
	v_fma_mix_f32 v19, v59, v36, v19 op_sel:[1,0,0] op_sel_hi:[1,0,0]
	v_fma_mix_f32 v20, v60, v36, v20 op_sel_hi:[1,0,0]
	v_fma_mix_f32 v21, v60, v36, v21 op_sel:[1,0,0] op_sel_hi:[1,0,0]
	v_fma_mix_f32 v22, v61, v36, v22 op_sel_hi:[1,0,0]
	v_fma_mix_f32 v23, v61, v36, v23 op_sel:[1,0,0] op_sel_hi:[1,0,0]
	v_cvt_scalef32_pk_f16_fp8 v58, v42, 1.0
	v_cvt_scalef32_pk_f16_fp8 v59, v42, 1.0 op_sel:[1,0,0]
	v_cvt_scalef32_pk_f16_fp8 v60, v43, 1.0
	v_cvt_scalef32_pk_f16_fp8 v61, v43, 1.0 op_sel:[1,0,0]
	v_fma_mix_f32 v24, v58, v36, v24 op_sel_hi:[1,0,0]
	v_fma_mix_f32 v25, v58, v36, v25 op_sel:[1,0,0] op_sel_hi:[1,0,0]
	v_fma_mix_f32 v26, v59, v36, v26 op_sel_hi:[1,0,0]
	v_fma_mix_f32 v27, v59, v36, v27 op_sel:[1,0,0] op_sel_hi:[1,0,0]
	v_fma_mix_f32 v28, v60, v36, v28 op_sel_hi:[1,0,0]
	v_fma_mix_f32 v29, v60, v36, v29 op_sel:[1,0,0] op_sel_hi:[1,0,0]
	v_fma_mix_f32 v30, v61, v36, v30 op_sel_hi:[1,0,0]
	v_fma_mix_f32 v31, v61, v36, v31 op_sel:[1,0,0] op_sel_hi:[1,0,0]
	s_waitcnt vmcnt(0)
	v_cvt_scalef32_pk_f16_fp8 v58, v44, 1.0
	v_cvt_scalef32_pk_f16_fp8 v59, v44, 1.0 op_sel:[1,0,0]
	v_cvt_scalef32_pk_f16_fp8 v60, v45, 1.0
	v_cvt_scalef32_pk_f16_fp8 v61, v45, 1.0 op_sel:[1,0,0]
	v_fma_mix_f32 v16, v58, v37, v16 op_sel_hi:[1,0,0]
	v_fma_mix_f32 v17, v58, v37, v17 op_sel:[1,0,0] op_sel_hi:[1,0,0]
	v_fma_mix_f32 v18, v59, v37, v18 op_sel_hi:[1,0,0]
	v_fma_mix_f32 v19, v59, v37, v19 op_sel:[1,0,0] op_sel_hi:[1,0,0]
	v_fma_mix_f32 v20, v60, v37, v20 op_sel_hi:[1,0,0]
	v_fma_mix_f32 v21, v60, v37, v21 op_sel:[1,0,0] op_sel_hi:[1,0,0]
	v_fma_mix_f32 v22, v61, v37, v22 op_sel_hi:[1,0,0]
	v_fma_mix_f32 v23, v61, v37, v23 op_sel:[1,0,0] op_sel_hi:[1,0,0]
	v_cvt_scalef32_pk_f16_fp8 v58, v46, 1.0
	v_cvt_scalef32_pk_f16_fp8 v59, v46, 1.0 op_sel:[1,0,0]
	v_cvt_scalef32_pk_f16_fp8 v60, v47, 1.0
	v_cvt_scalef32_pk_f16_fp8 v61, v47, 1.0 op_sel:[1,0,0]
	v_fma_mix_f32 v24, v58, v37, v24 op_sel_hi:[1,0,0]
	v_fma_mix_f32 v25, v58, v37, v25 op_sel:[1,0,0] op_sel_hi:[1,0,0]
	v_fma_mix_f32 v26, v59, v37, v26 op_sel_hi:[1,0,0]
	v_fma_mix_f32 v27, v59, v37, v27 op_sel:[1,0,0] op_sel_hi:[1,0,0]
	v_fma_mix_f32 v28, v60, v37, v28 op_sel_hi:[1,0,0]
	v_fma_mix_f32 v29, v60, v37, v29 op_sel:[1,0,0] op_sel_hi:[1,0,0]
	v_fma_mix_f32 v30, v61, v37, v30 op_sel_hi:[1,0,0]
	v_fma_mix_f32 v31, v61, v37, v31 op_sel:[1,0,0] op_sel_hi:[1,0,0]
	s_branch .Lagg_epi
.Lagg_B_half:
	ds_swizzle_b32 v32, v5 offset:swizzle(BITMASK_PERM, "pp100")
	ds_swizzle_b32 v33, v5 offset:swizzle(BITMASK_PERM, "pp101")
	s_waitcnt lgkmcnt(0)
	v_or_b32_e32 v32, v32, v1
	v_or_b32_e32 v33, v33, v1
	global_load_ushort v36, v32, s[6:7]
	global_load_ushort v37, v33, s[6:7]
	v_lshlrev_b32_e32 v32, 3, v32
	v_lshlrev_b32_e32 v33, 3, v33
	global_load_dwordx4 v[40:43], v32, s[4:5]
	global_load_dwordx4 v[44:47], v33, s[4:5]
	s_waitcnt vmcnt(2)
	v_fma_mix_f32 v36, v36, 1.0, v9 op_sel_hi:[1,0,0]
	v_fma_mix_f32 v37, v37, 1.0, v9 op_sel_hi:[1,0,0]
	v_mul_f32_e32 v58, 0x3e4ccccd, v36
	v_mul_f32_e32 v59, 0x3e4ccccd, v37
	v_max_f32_e32 v36, v36, v58
	v_max_f32_e32 v37, v37, v59
	v_max3_f32 v12, v13, v36, v37
	v_sub_f32_e32 v57, v13, v12
	v_sub_f32_e32 v36, v36, v12
	v_sub_f32_e32 v37, v37, v12
	v_exp_f32_e32 v57, v57
	v_exp_f32_e32 v36, v36
	v_exp_f32_e32 v37, v37
	v_fma_f32 v14, v14, v57, v36
	v_mul_f32_e32 v16, v16, v57
	v_mul_f32_e32 v17, v17, v57
	v_mul_f32_e32 v18, v18, v57
	v_mul_f32_e32 v19, v19, v57
	v_mul_f32_e32 v20, v20, v57
	v_mul_f32_e32 v21, v21, v57
	v_mul_f32_e32 v22, v22, v57
	v_mul_f32_e32 v23, v23, v57
	v_mul_f32_e32 v24, v24, v57
	v_mul_f32_e32 v25, v25, v57
	v_mul_f32_e32 v26, v26, v57
	v_mul_f32_e32 v27, v27, v57
	v_mul_f32_e32 v28, v28, v57
	v_mul_f32_e32 v29, v29, v57
	v_mul_f32_e32 v30, v30, v57
	v_mul_f32_e32 v31, v31, v57
	v_add_f32_e32 v14, v14, v37
	s_waitcnt vmcnt(1)
	v_cvt_scalef32_pk_f16_fp8 v58, v40, 1.0
	v_cvt_scalef32_pk_f16_fp8 v59, v40, 1.0 op_sel:[1,0,0]
	v_cvt_scalef32_pk_f16_fp8 v60, v41, 1.0
	v_cvt_scalef32_pk_f16_fp8 v61, v41, 1.0 op_sel:[1,0,0]
	v_fma_mix_f32 v16, v58, v36, v16 op_sel_hi:[1,0,0]
	v_fma_mix_f32 v17, v58, v36, v17 op_sel:[1,0,0] op_sel_hi:[1,0,0]
	v_fma_mix_f32 v18, v59, v36, v18 op_sel_hi:[1,0,0]
	v_fma_mix_f32 v19, v59, v36, v19 op_sel:[1,0,0] op_sel_hi:[1,0,0]
	v_fma_mix_f32 v20, v60, v36, v20 op_sel_hi:[1,0,0]
	v_fma_mix_f32 v21, v60, v36, v21 op_sel:[1,0,0] op_sel_hi:[1,0,0]
	v_fma_mix_f32 v22, v61, v36, v22 op_sel_hi:[1,0,0]
	v_fma_mix_f32 v23, v61, v36, v23 op_sel:[1,0,0] op_sel_hi:[1,0,0]
	v_cvt_scalef32_pk_f16_fp8 v58, v42, 1.0
	v_cvt_scalef32_pk_f16_fp8 v59, v42, 1.0 op_sel:[1,0,0]
	v_cvt_scalef32_pk_f16_fp8 v60, v43, 1.0
	v_cvt_scalef32_pk_f16_fp8 v61, v43, 1.0 op_sel:[1,0,0]
	v_fma_mix_f32 v24, v58, v36, v24 op_sel_hi:[1,0,0]
	v_fma_mix_f32 v25, v58, v36, v25 op_sel:[1,0,0] op_sel_hi:[1,0,0]
	v_fma_mix_f32 v26, v59, v36, v26 op_sel_hi:[1,0,0]
	v_fma_mix_f32 v27, v59, v36, v27 op_sel:[1,0,0] op_sel_hi:[1,0,0]
	v_fma_mix_f32 v28, v60, v36, v28 op_sel_hi:[1,0,0]
	v_fma_mix_f32 v29, v60, v36, v29 op_sel:[1,0,0] op_sel_hi:[1,0,0]
	v_fma_mix_f32 v30, v61, v36, v30 op_sel_hi:[1,0,0]
	v_fma_mix_f32 v31, v61, v36, v31 op_sel:[1,0,0] op_sel_hi:[1,0,0]
	s_waitcnt vmcnt(0)
	v_cvt_scalef32_pk_f16_fp8 v58, v44, 1.0
	v_cvt_scalef32_pk_f16_fp8 v59, v44, 1.0 op_sel:[1,0,0]
	v_cvt_scalef32_pk_f16_fp8 v60, v45, 1.0
	v_cvt_scalef32_pk_f16_fp8 v61, v45, 1.0 op_sel:[1,0,0]
	v_fma_mix_f32 v16, v58, v37, v16 op_sel_hi:[1,0,0]
	v_fma_mix_f32 v17, v58, v37, v17 op_sel:[1,0,0] op_sel_hi:[1,0,0]
	v_fma_mix_f32 v18, v59, v37, v18 op_sel_hi:[1,0,0]
	v_fma_mix_f32 v19, v59, v37, v19 op_sel:[1,0,0] op_sel_hi:[1,0,0]
	v_fma_mix_f32 v20, v60, v37, v20 op_sel_hi:[1,0,0]
	v_fma_mix_f32 v21, v60, v37, v21 op_sel:[1,0,0] op_sel_hi:[1,0,0]
	v_fma_mix_f32 v22, v61, v37, v22 op_sel_hi:[1,0,0]
	v_fma_mix_f32 v23, v61, v37, v23 op_sel:[1,0,0] op_sel_hi:[1,0,0]
	v_cvt_scalef32_pk_f16_fp8 v58, v46, 1.0
	v_cvt_scalef32_pk_f16_fp8 v59, v46, 1.0 op_sel:[1,0,0]
	v_cvt_scalef32_pk_f16_fp8 v60, v47, 1.0
	v_cvt_scalef32_pk_f16_fp8 v61, v47, 1.0 op_sel:[1,0,0]
	v_fma_mix_f32 v24, v58, v37, v24 op_sel_hi:[1,0,0]
	v_fma_mix_f32 v25, v58, v37, v25 op_sel:[1,0,0] op_sel_hi:[1,0,0]
	v_fma_mix_f32 v26, v59, v37, v26 op_sel_hi:[1,0,0]
	v_fma_mix_f32 v27, v59, v37, v27 op_sel:[1,0,0] op_sel_hi:[1,0,0]
	v_fma_mix_f32 v28, v60, v37, v28 op_sel_hi:[1,0,0]
	v_fma_mix_f32 v29, v60, v37, v29 op_sel:[1,0,0] op_sel_hi:[1,0,0]
	v_fma_mix_f32 v30, v61, v37, v30 op_sel_hi:[1,0,0]
	v_fma_mix_f32 v31, v61, v37, v31 op_sel:[1,0,0] op_sel_hi:[1,0,0]
.Lagg_epi:
	s_and_saveexec_b64 s[32:33], s[36:37]
	v_rcp_f32_e32 v57, v14
	ds_read_b128 v[32:35], v62 offset:0
	ds_read_b128 v[36:39], v62 offset:16
	ds_read_b128 v[40:43], v62 offset:512
	ds_read_b128 v[44:47], v62 offset:528
	ds_read_b128 v[48:51], v62 offset:1024
	ds_read_b128 v[52:55], v62 offset:1040
	s_waitcnt lgkmcnt(2)
	v_mul_f32_e32 v16, v16, v57
	v_mul_f32_e32 v17, v17, v57
	v_mul_f32_e32 v18, v18, v57
	v_mul_f32_e32 v19, v19, v57
	v_mul_f32_e32 v20, v20, v57
	v_mul_f32_e32 v21, v21, v57
	v_mul_f32_e32 v22, v22, v57
	v_mul_f32_e32 v23, v23, v57
	v_fma_f32 v16, v16, v32, v40
	v_fma_f32 v17, v17, v33, v41
	v_fma_f32 v18, v18, v34, v42
	v_fma_f32 v19, v19, v35, v43
	v_fma_f32 v20, v20, v36, v44
	v_fma_f32 v21, v21, v37, v45
	v_fma_f32 v22, v22, v38, v46
	v_fma_f32 v23, v23, v39, v47
	ds_read_b128 v[32:35], v62 offset:1536
	ds_read_b128 v[36:39], v62 offset:1552
	v_mul_f32_e32 v59, 0x3fb8aa3b, v16
	v_mul_f32_e32 v60, 0x3fb8aa3b, v17
	v_mul_f32_e32 v61, 0x3fb8aa3b, v18
	v_mul_f32_e32 v67, 0x3fb8aa3b, v19
	v_exp_f32_e32 v59, v59
	v_exp_f32_e32 v60, v60
	v_exp_f32_e32 v61, v61
	v_exp_f32_e32 v67, v67
	v_add_f32_e32 v59, -1.0, v59
	v_add_f32_e32 v60, -1.0, v60
	v_add_f32_e32 v61, -1.0, v61
	v_add_f32_e32 v67, -1.0, v67
	v_med3_f32 v16, v16, v59, 0
	v_med3_f32 v17, v17, v60, 0
	v_med3_f32 v18, v18, v61, 0
	v_med3_f32 v19, v19, v67, 0
	v_cvt_f16_f32_e32 v59, v16
	v_cvt_f16_f32_e32 v60, v17
	v_cvt_f16_f32_e32 v61, v18
	v_cvt_f16_f32_e32 v67, v19
	ds_write_b16 v3, v59
	ds_write_b16 v3, v60 offset:16
	ds_write_b16 v3, v61 offset:32
	ds_write_b16 v3, v67 offset:48
	v_mul_f32_e32 v59, 0x3fb8aa3b, v20
	v_mul_f32_e32 v60, 0x3fb8aa3b, v21
	v_mul_f32_e32 v61, 0x3fb8aa3b, v22
	v_mul_f32_e32 v67, 0x3fb8aa3b, v23
	v_exp_f32_e32 v59, v59
	v_exp_f32_e32 v60, v60
	v_exp_f32_e32 v61, v61
	v_exp_f32_e32 v67, v67
	v_add_f32_e32 v59, -1.0, v59
	v_add_f32_e32 v60, -1.0, v60
	v_add_f32_e32 v61, -1.0, v61
	v_add_f32_e32 v67, -1.0, v67
	v_med3_f32 v20, v20, v59, 0
	v_med3_f32 v21, v21, v60, 0
	v_med3_f32 v22, v22, v61, 0
	v_med3_f32 v23, v23, v67, 0
	v_cvt_f16_f32_e32 v59, v20
	v_cvt_f16_f32_e32 v60, v21
	v_cvt_f16_f32_e32 v61, v22
	v_cvt_f16_f32_e32 v67, v23
	ds_write_b16 v3, v59 offset:64
	ds_write_b16 v3, v60 offset:80
	ds_write_b16 v3, v61 offset:96
	ds_write_b16 v3, v67 offset:112
	s_waitcnt lgkmcnt(0)
	v_mul_f32_e32 v56, v16, v48
	v_mul_f32_e32 v58, v16, v32
	v_fmac_f32_e32 v56, v17, v49
	v_fmac_f32_e32 v58, v17, v33
	v_fmac_f32_e32 v56, v18, v50
	v_fmac_f32_e32 v58, v18, v34
	v_fmac_f32_e32 v56, v19, v51
	v_fmac_f32_e32 v58, v19, v35
	v_fmac_f32_e32 v56, v20, v52
	v_fmac_f32_e32 v58, v20, v36
	v_fmac_f32_e32 v56, v21, v53
	v_fmac_f32_e32 v58, v21, v37
	v_fmac_f32_e32 v56, v22, v54
	v_fmac_f32_e32 v58, v22, v38
	v_fmac_f32_e32 v56, v23, v55
	v_fmac_f32_e32 v58, v23, v39
	ds_read_b128 v[32:35], v62 offset:32
	ds_read_b128 v[36:39], v62 offset:48
	ds_read_b128 v[40:43], v62 offset:544
	ds_read_b128 v[44:47], v62 offset:560
	ds_read_b128 v[48:51], v62 offset:1056
	ds_read_b128 v[52:55], v62 offset:1072
	s_waitcnt lgkmcnt(2)
	v_mul_f32_e32 v24, v24, v57
	v_mul_f32_e32 v25, v25, v57
	v_mul_f32_e32 v26, v26, v57
	v_mul_f32_e32 v27, v27, v57
	v_mul_f32_e32 v28, v28, v57
	v_mul_f32_e32 v29, v29, v57
	v_mul_f32_e32 v30, v30, v57
	v_mul_f32_e32 v31, v31, v57
	v_fma_f32 v24, v24, v32, v40
	v_fma_f32 v25, v25, v33, v41
	v_fma_f32 v26, v26, v34, v42
	v_fma_f32 v27, v27, v35, v43
	v_fma_f32 v28, v28, v36, v44
	v_fma_f32 v29, v29, v37, v45
	v_fma_f32 v30, v30, v38, v46
	v_fma_f32 v31, v31, v39, v47
	ds_read_b128 v[32:35], v62 offset:1568
	ds_read_b128 v[36:39], v62 offset:1584
	v_mul_f32_e32 v59, 0x3fb8aa3b, v24
	v_mul_f32_e32 v60, 0x3fb8aa3b, v25
	v_mul_f32_e32 v61, 0x3fb8aa3b, v26
	v_mul_f32_e32 v67, 0x3fb8aa3b, v27
	v_exp_f32_e32 v59, v59
	v_exp_f32_e32 v60, v60
	v_exp_f32_e32 v61, v61
	v_exp_f32_e32 v67, v67
	v_add_f32_e32 v59, -1.0, v59
	v_add_f32_e32 v60, -1.0, v60
	v_add_f32_e32 v61, -1.0, v61
	v_add_f32_e32 v67, -1.0, v67
	v_med3_f32 v24, v24, v59, 0
	v_med3_f32 v25, v25, v60, 0
	v_med3_f32 v26, v26, v61, 0
	v_med3_f32 v27, v27, v67, 0
	v_cvt_f16_f32_e32 v59, v24
	v_cvt_f16_f32_e32 v60, v25
	v_cvt_f16_f32_e32 v61, v26
	v_cvt_f16_f32_e32 v67, v27
	ds_write_b16 v3, v59 offset:128
	ds_write_b16 v3, v60 offset:144
	ds_write_b16 v3, v61 offset:160
	ds_write_b16 v3, v67 offset:176
	v_mul_f32_e32 v59, 0x3fb8aa3b, v28
	v_mul_f32_e32 v60, 0x3fb8aa3b, v29
	v_mul_f32_e32 v61, 0x3fb8aa3b, v30
	v_mul_f32_e32 v67, 0x3fb8aa3b, v31
	v_exp_f32_e32 v59, v59
	v_exp_f32_e32 v60, v60
	v_exp_f32_e32 v61, v61
	v_exp_f32_e32 v67, v67
	v_add_f32_e32 v59, -1.0, v59
	v_add_f32_e32 v60, -1.0, v60
	v_add_f32_e32 v61, -1.0, v61
	v_add_f32_e32 v67, -1.0, v67
	v_med3_f32 v28, v28, v59, 0
	v_med3_f32 v29, v29, v60, 0
	v_med3_f32 v30, v30, v61, 0
	v_med3_f32 v31, v31, v67, 0
	v_cvt_f16_f32_e32 v59, v28
	v_cvt_f16_f32_e32 v60, v29
	v_cvt_f16_f32_e32 v61, v30
	v_cvt_f16_f32_e32 v67, v31
	ds_write_b16 v3, v59 offset:192
	ds_write_b16 v3, v60 offset:208
	ds_write_b16 v3, v61 offset:224
	ds_write_b16 v3, v67 offset:240
	s_waitcnt lgkmcnt(0)
	v_fmac_f32_e32 v56, v24, v48
	v_fmac_f32_e32 v58, v24, v32
	v_fmac_f32_e32 v56, v25, v49
	v_fmac_f32_e32 v58, v25, v33
	v_fmac_f32_e32 v56, v26, v50
	v_fmac_f32_e32 v58, v26, v34
	v_fmac_f32_e32 v56, v27, v51
	v_fmac_f32_e32 v58, v27, v35
	v_fmac_f32_e32 v56, v28, v52
	v_fmac_f32_e32 v58, v28, v36
	v_fmac_f32_e32 v56, v29, v53
	v_fmac_f32_e32 v58, v29, v37
	v_fmac_f32_e32 v56, v30, v54
	v_fmac_f32_e32 v58, v30, v38
	v_fmac_f32_e32 v56, v31, v55
	v_fmac_f32_e32 v58, v31, v39
	s_nop 1
	v_add_f32_dpp v56, v56, v56 quad_perm:[1,0,3,2] row_mask:0xf bank_mask:0xf
	v_add_f32_dpp v58, v58, v58 quad_perm:[1,0,3,2] row_mask:0xf bank_mask:0xf
	s_nop 0
	v_add_f32_dpp v56, v56, v56 quad_perm:[2,3,0,1] row_mask:0xf bank_mask:0xf
	v_add_f32_dpp v58, v58, v58 quad_perm:[2,3,0,1] row_mask:0xf bank_mask:0xf
	s_nop 0
	ds_swizzle_b32 v59, v56 offset:swizzle(SWAP,4)
	ds_swizzle_b32 v60, v58 offset:swizzle(SWAP,4)
	s_waitcnt lgkmcnt(0)
	v_add_f32_e32 v56, v56, v59
	v_add_f32_e32 v58, v58, v60
	s_and_b64 exec, exec, s[34:35]
	global_store_dword v4, v56, s[20:21]
	global_store_dword v4, v58, s[22:23]
	s_mov_b64 exec, s[32:33]
	s_waitcnt lgkmcnt(0)
	ds_read_b128 v[32:35], v63
	ds_read_b128 v[36:39], v63 offset:16
	s_ashr_i32 s27, s26, 3
	s_lshl_b32 s27, s27, 11
	v_and_b32_e32 v40, 63, v0
	v_lshlrev_b32_e32 v40, 5, v40
	v_add_u32_e32 v40, s27, v40
	s_waitcnt lgkmcnt(0)
	global_store_dwordx4 v40, v[32:35], s[18:19]
	global_store_dwordx4 v40, v[36:39], s[18:19] offset:16

	.amdhsa_kernel _Z11agg1_kernelPKDF16_PKfS2_PKiS4_S2_S2_PDF16_PfS6_i
		.amdhsa_group_segment_fixed_size 10240
		.amdhsa_private_segment_fixed_size 0
		.amdhsa_kernarg_size 84
		.amdhsa_user_sgpr_count 2
		.amdhsa_user_sgpr_dispatch_ptr 0
		.amdhsa_user_sgpr_queue_ptr 0
		.amdhsa_user_sgpr_kernarg_segment_ptr 1
		.amdhsa_user_sgpr_dispatch_id 0
		.amdhsa_user_sgpr_kernarg_preload_length 0
		.amdhsa_user_sgpr_kernarg_preload_offset 0
		.amdhsa_user_sgpr_private_segment_size 0
		.amdhsa_uses_dynamic_stack 0
		.amdhsa_enable_private_segment 0
		.amdhsa_system_sgpr_workgroup_id_x 1
		.amdhsa_system_sgpr_workgroup_id_y 0
		.amdhsa_system_sgpr_workgroup_id_z 0
		.amdhsa_system_sgpr_workgroup_info 0
		.amdhsa_system_vgpr_workitem_id 0
		.amdhsa_next_free_vgpr 70
		.amdhsa_next_free_sgpr 44
		.amdhsa_accum_offset 72
		.amdhsa_reserve_vcc 1
		.amdhsa_float_round_mode_32 0
		.amdhsa_float_round_mode_16_64 0
		.amdhsa_float_denorm_mode_32 3
		.amdhsa_float_denorm_mode_16_64 3
		.amdhsa_dx10_clamp 1
		.amdhsa_ieee_mode 1
		.amdhsa_fp16_overflow 0
		.amdhsa_tg_split 0
		.amdhsa_exception_fp_ieee_invalid_op 0
		.amdhsa_exception_fp_denorm_src 0
		.amdhsa_exception_fp_ieee_div_zero 0
		.amdhsa_exception_fp_ieee_overflow 0
		.amdhsa_exception_fp_ieee_underflow 0
		.amdhsa_exception_fp_ieee_inexact 0
		.amdhsa_exception_int_div_zero 0
	.end_amdhsa_kernel

amdhsa.kernels:
  - .agpr_count:     0
    .args:
      - .actual_access:  read_only
        .address_space:  global
        .offset:         0
        .size:           8
        .value_kind:     global_buffer
      - .actual_access:  read_only
        .address_space:  global
        .offset:         8
        .size:           8
        .value_kind:     global_buffer
      - .actual_access:  read_only
        .address_space:  global
        .offset:         16
        .size:           8
        .value_kind:     global_buffer
      - .actual_access:  read_only
        .address_space:  global
        .offset:         24
        .size:           8
        .value_kind:     global_buffer
      - .actual_access:  read_only
        .address_space:  global
        .offset:         32
        .size:           8
        .value_kind:     global_buffer
      - .actual_access:  read_only
        .address_space:  global
        .offset:         40
        .size:           8
        .value_kind:     global_buffer
      - .actual_access:  read_only
        .address_space:  global
        .offset:         48
        .size:           8
        .value_kind:     global_buffer
      - .actual_access:  read_only
        .address_space:  global
        .offset:         56
        .size:           8
        .value_kind:     global_buffer
      - .actual_access:  read_only
        .address_space:  global
        .offset:         64
        .size:           8
        .value_kind:     global_buffer
      - .actual_access:  read_only
        .address_space:  global
        .offset:         72
        .size:           8
        .value_kind:     global_buffer
      - .actual_access:  read_only
        .address_space:  global
        .offset:         80
        .size:           8
        .value_kind:     global_buffer
      - .actual_access:  read_only
        .address_space:  global
        .offset:         88
        .size:           8
        .value_kind:     global_buffer
      - .actual_access:  read_only
        .address_space:  global
        .offset:         96
        .size:           8
        .value_kind:     global_buffer
      - .actual_access:  write_only
        .address_space:  global
        .offset:         104
        .size:           8
        .value_kind:     global_buffer
      - .actual_access:  write_only
        .address_space:  global
        .offset:         112
        .size:           8
        .value_kind:     global_buffer
      - .actual_access:  write_only
        .address_space:  global
        .offset:         120
        .size:           8
        .value_kind:     global_buffer
      - .actual_access:  write_only
        .address_space:  global
        .offset:         128
        .size:           8
        .value_kind:     global_buffer
      - .actual_access:  write_only
        .address_space:  global
        .offset:         136
        .size:           8
        .value_kind:     global_buffer
      - .actual_access:  write_only
        .address_space:  global
        .offset:         144
        .size:           8
        .value_kind:     global_buffer
      - .actual_access:  write_only
        .address_space:  global
        .offset:         152
        .size:           8
        .value_kind:     global_buffer
      - .actual_access:  write_only
        .address_space:  global
        .offset:         160
        .size:           8
        .value_kind:     global_buffer
      - .actual_access:  write_only
        .address_space:  global
        .offset:         168
        .size:           8
        .value_kind:     global_buffer
      - .actual_access:  read_only
        .address_space:  global
        .offset:         176
        .size:           8
        .value_kind:     global_buffer
    .group_segment_fixed_size: 29696
    .kernarg_segment_align: 8
    .kernarg_segment_size: 184
    .language:       OpenCL C
    .language_version:
      - 2
      - 0
    .max_flat_workgroup_size: 512
    .name:           _Z12front_kernelPKiS0_PKfS2_S2_S2_S2_S2_S2_S2_S2_S2_S2_PjS3_PiS4_PDF16_PfS6_S4_S5_S0_
    .private_segment_fixed_size: 0
    .sgpr_count:     30
    .sgpr_spill_count: 0
    .symbol:         _Z12front_kernelPKiS0_PKfS2_S2_S2_S2_S2_S2_S2_S2_S2_S2_PjS3_PiS4_PDF16_PfS6_S4_S5_S0_.kd
    .uniform_work_group_size: 1
    .uses_dynamic_stack: false
    .vgpr_count:     80
    .vgpr_spill_count: 0
    .wavefront_size: 64
  - .agpr_count:     0
    .args:
      - .actual_access:  read_only
        .address_space:  global
        .offset:         0
        .size:           8
        .value_kind:     global_buffer
      - .actual_access:  read_only
        .address_space:  global
        .offset:         8
        .size:           8
        .value_kind:     global_buffer
      - .actual_access:  write_only
        .address_space:  global
        .offset:         16
        .size:           8
        .value_kind:     global_buffer
      - .actual_access:  write_only
        .address_space:  global
        .offset:         24
        .size:           8
        .value_kind:     global_buffer
      - .actual_access:  write_only
        .address_space:  global
        .offset:         32
        .size:           8
        .value_kind:     global_buffer
      - .actual_access:  read_only
        .address_space:  global
        .offset:         40
        .size:           8
        .value_kind:     global_buffer
      - .actual_access:  read_only
        .address_space:  global
        .offset:         48
        .size:           8
        .value_kind:     global_buffer
      - .actual_access:  write_only
        .address_space:  global
        .offset:         56
        .size:           8
        .value_kind:     global_buffer
      - .actual_access:  write_only
        .address_space:  global
        .offset:         64
        .size:           8
        .value_kind:     global_buffer
    .group_segment_fixed_size: 40960
    .kernarg_segment_align: 8
    .kernarg_segment_size: 72
    .language:       OpenCL C
    .language_version:
      - 2
      - 0
    .max_flat_workgroup_size: 512
    .name:           _Z13second_kernelPKfPKDF16_PDF16_PfS4_PKjPKiPiS9_
    .private_segment_fixed_size: 0
    .sgpr_count:     29
    .sgpr_spill_count: 0
    .symbol:         _Z13second_kernelPKfPKDF16_PDF16_PfS4_PKjPKiPiS9_.kd
    .uniform_work_group_size: 1
    .uses_dynamic_stack: false
    .vgpr_count:     64
    .vgpr_spill_count: 0
    .wavefront_size: 64
  - .agpr_count:     0
    .args:
      - .actual_access:  read_only
        .address_space:  global
        .offset:         0
        .size:           8
        .value_kind:     global_buffer
      - .actual_access:  read_only
        .address_space:  global
        .offset:         8
        .size:           8
        .value_kind:     global_buffer
      - .actual_access:  read_only
        .address_space:  global
        .offset:         16
        .size:           8
        .value_kind:     global_buffer
      - .actual_access:  read_only
        .address_space:  global
        .offset:         24
        .size:           8
        .value_kind:     global_buffer
      - .actual_access:  read_only
        .address_space:  global
        .offset:         32
        .size:           8
        .value_kind:     global_buffer
      - .actual_access:  read_only
        .address_space:  global
        .offset:         40
        .size:           8
        .value_kind:     global_buffer
      - .actual_access:  read_only
        .address_space:  global
        .offset:         48
        .size:           8
        .value_kind:     global_buffer
      - .actual_access:  write_only
        .address_space:  global
        .offset:         56
        .size:           8
        .value_kind:     global_buffer
      - .actual_access:  write_only
        .address_space:  global
        .offset:         64
        .size:           8
        .value_kind:     global_buffer
      - .actual_access:  write_only
        .address_space:  global
        .offset:         72
        .size:           8
        .value_kind:     global_buffer
      - .offset:         80
        .size:           4
        .value_kind:     by_value
    .group_segment_fixed_size: 10240
    .kernarg_segment_align: 8
    .kernarg_segment_size: 84
    .language:       OpenCL C
    .language_version:
      - 2
      - 0
    .max_flat_workgroup_size: 256
    .name:           _Z11agg1_kernelPKDF16_PKfS2_PKiS4_S2_S2_PDF16_PfS6_i
    .private_segment_fixed_size: 0
    .sgpr_count:     50
    .sgpr_spill_count: 0
    .symbol:         _Z11agg1_kernelPKDF16_PKfS2_PKiS4_S2_S2_PDF16_PfS6_i.kd
    .uniform_work_group_size: 1
    .uses_dynamic_stack: false
    .vgpr_count:     70
    .vgpr_spill_count: 0
    .wavefront_size: 64
  - .agpr_count:     0
    .args:
      - .actual_access:  read_only
        .address_space:  global
        .offset:         0
        .size:           8
        .value_kind:     global_buffer
      - .actual_access:  read_only
        .address_space:  global
        .offset:         8
        .size:           8
        .value_kind:     global_buffer
      - .actual_access:  read_only
        .address_space:  global
        .offset:         16
        .size:           8
        .value_kind:     global_buffer
      - .actual_access:  read_only
        .address_space:  global
        .offset:         24
        .size:           8
        .value_kind:     global_buffer
      - .actual_access:  read_only
        .address_space:  global
        .offset:         32
        .size:           8
        .value_kind:     global_buffer
      - .actual_access:  write_only
        .address_space:  global
        .offset:         40
        .size:           8
        .value_kind:     global_buffer
      - .offset:         48
        .size:           4
        .value_kind:     by_value
    .group_segment_fixed_size: 0
    .kernarg_segment_align: 8
    .kernarg_segment_size: 52
    .language:       OpenCL C
    .language_version:
      - 2
      - 0
    .max_flat_workgroup_size: 256
    .name:           _Z13stats2_kernelPKiS0_PKfS2_S0_P15HIP_vector_typeIfLj4EEi
    .private_segment_fixed_size: 0
    .sgpr_count:     27
    .sgpr_spill_count: 0
    .symbol:         _Z13stats2_kernelPKiS0_PKfS2_S0_P15HIP_vector_typeIfLj4EEi.kd
    .uniform_work_group_size: 1
    .uses_dynamic_stack: false
    .vgpr_count:     32
    .vgpr_spill_count: 0
    .wavefront_size: 64
  - .agpr_count:     0
    .args:
      - .actual_access:  read_only
        .address_space:  global
        .offset:         0
        .size:           8
        .value_kind:     global_buffer
      - .actual_access:  read_only
        .address_space:  global
        .offset:         8
        .size:           8
        .value_kind:     global_buffer
      - .actual_access:  read_only
        .address_space:  global
        .offset:         16
        .size:           8
        .value_kind:     global_buffer
      - .actual_access:  read_only
        .address_space:  global
        .offset:         24
        .size:           8
        .value_kind:     global_buffer
      - .actual_access:  read_only
        .address_space:  global
        .offset:         32
        .size:           8
        .value_kind:     global_buffer
      - .actual_access:  write_only
        .address_space:  global
        .offset:         40
        .size:           8
        .value_kind:     global_buffer
      - .offset:         48
        .size:           4
        .value_kind:     by_value
    .group_segment_fixed_size: 69728
    .kernarg_segment_align: 8
    .kernarg_segment_size: 52
    .language:       OpenCL C
    .language_version:
      - 2
      - 0
    .max_flat_workgroup_size: 1024
    .name:           _Z12pool2_kernelPKjPKiPKfPK15HIP_vector_typeIfLj4EEPKDF16_Pfi
    .private_segment_fixed_size: 0
    .sgpr_count:     26
    .sgpr_spill_count: 0
    .symbol:         _Z12pool2_kernelPKjPKiPKfPK15HIP_vector_typeIfLj4EEPKDF16_Pfi.kd
    .uniform_work_group_size: 1
    .uses_dynamic_stack: false
    .vgpr_count:     123
    .vgpr_spill_count: 0
    .wavefront_size: 64
  - .agpr_count:     0
    .args:
      - .actual_access:  read_only
        .address_space:  global
        .offset:         0
        .size:           8
        .value_kind:     global_buffer
      - .actual_access:  read_only
        .address_space:  global
        .offset:         8
        .size:           8
        .value_kind:     global_buffer
      - .actual_access:  read_only
        .address_space:  global
        .offset:         16
        .size:           8
        .value_kind:     global_buffer
      - .actual_access:  read_only
        .address_space:  global
        .offset:         24
        .size:           8
        .value_kind:     global_buffer
      - .actual_access:  read_only
        .address_space:  global
        .offset:         32
        .size:           8
        .value_kind:     global_buffer
      - .actual_access:  read_only
        .address_space:  global
        .offset:         40
        .size:           8
        .value_kind:     global_buffer
      - .actual_access:  read_only
        .address_space:  global
        .offset:         48
        .size:           8
        .value_kind:     global_buffer
      - .actual_access:  read_only
        .address_space:  global
        .offset:         56
        .size:           8
        .value_kind:     global_buffer
      - .actual_access:  write_only
        .address_space:  global
        .offset:         64
        .size:           8
        .value_kind:     global_buffer
    .group_segment_fixed_size: 9472
    .kernarg_segment_align: 8
    .kernarg_segment_size: 72
    .language:       OpenCL C
    .language_version:
      - 2
      - 0
    .max_flat_workgroup_size: 1024
    .name:           _Z10mlp_kernelPKfPKiS0_S0_S0_S0_S0_S0_Pf
    .private_segment_fixed_size: 0
    .sgpr_count:     38
    .sgpr_spill_count: 0
    .symbol:         _Z10mlp_kernelPKfPKiS0_S0_S0_S0_S0_S0_Pf.kd
    .uniform_work_group_size: 1
    .uses_dynamic_stack: false
    .vgpr_count:     64
    .vgpr_spill_count: 0
    .wavefront_size: 64
